# P9 epilogue: per-store 64-bit address VALU chains (192 VALU/unit) replaced by one lane offset + SGPR-base global_store (SALU offsets); plus rope prefetch
# speedup vs baseline: 1.0001x; 1.0001x over previous
; __host__ __device__ __forceinline__ int qkv_row(int pos, int g) { const int dsh = 2 * g; return ((pos & ((1 << dsh) - 1)) << (12 - dsh)) + (pos >> dsh); }
; __device__ __forceinline__ u32x4 pack8(const f32x4 v0, const f32x4 v1) { u32x4 w; w.x = cvt_pk_bf16(v0[0], v0[1]); w.y = cvt_pk_bf16(v0[2], v0[3]); w.z = cvt_pk_bf16(v1[0], v1[1]); w.w = cvt_pk_bf16(v1[2], v1[3]); return w; }
; __host__ __device__ __forceinline__ size_t qkv_block(int typ, int g, int b, int h) { return (size_t)((((typ * 3 + g) * 16 + b) * 8 + h)) * (4096 * 64); }
;     __device__ __forceinline__ void operator()(const f32x4 (&acc)[2][2][4][2], const Unit& u, int wr, int wc, int fr, int fq) const {
;     ...
;         const int typ = (u.pn % 6) >> 1, gq_ = u.pn / 6;
;         const bool rl = (typ < 2) && ((wc & 1) == 0) && (fq < 2);
;         const float sc = (typ == 0) ? QSCALE : 1.0f;
; #pragma unroll
;         for (int ai = 0; ai < 2; ++ai)
; #pragma unroll
;         for (int mp = 0; mp < 2; ++mp) {
;             f32x4 csv[2], snv[2];
; #pragma unroll
;             for (int mm = 0; mm < 2; ++mm) { const int pos = (row0 + ai * HALF + (2 * mp + mm) * 16) & (SEQ - 1);
;                 csv[mm] = *(const f32x4*)(rope + pos * 8 + 4 * (fq & 1)); snv[mm] = *(const f32x4*)(rope + 4096 * 8 + pos * 8 + 4 * (fq & 1)); }
; #pragma unroll
;             for (int mm = 0; mm < 2; ++mm) {
;                 const int m = 2 * mp + mm, row = row0 + ai * HALF + m * 16;
;                 f32x4 cs = {1.f, 1.f, 1.f, 1.f}, sn = {0.f, 0.f, 0.f, 0.f};
;                 if (rl) { cs = csv[mm]; sn = snv[mm]; }
; #pragma unroll
;                 for (int bj = 0; bj < 2; ++bj) {
;                     const f32x4 x1 = acc[ai][bj][m][0], x2 = acc[ai][bj][m][1];
;                     const f32x4 r1 = (x1 * cs - x2 * sn) * sc, r2 = (x2 * cs + x1 * sn) * sc;
;                     { const int tok = row_off + row - fr + tr_, hh = 4 * (u.pn & 1) + 2 * bj + (wc >> 1);
;                       *(u32x4*)(O + qkv_block(typ, gq_, tok >> 12, hh) + (size_t)qkv_row(tok & (SEQ - 1), gq_) * 64 + 32 * (wc & 1) + 8 * tq_) = xpose4x16(pack8(r1, r2), sa_); }
.LBB0_1825:
	s_mul_hi_i32 s17, s51, 0x2aaaaaab
	s_lshl_b32 s19, s24, 8
	s_lshr_b32 s24, s17, 31
	s_add_i32 s17, s17, s24
	s_mul_i32 s24, s17, 6
	s_add_i32 s19, s19, s44
	s_mov_b32 s100, s19
	s_sub_i32 s28, s51, s24
	v_or_b32_e32 v128, s19, v176
	s_ashr_i32 s29, s28, 1
	s_cmp_lt_i32 s29, 2
	v_lshlrev_b32_e32 v185, 3, v128
	s_cselect_b64 s[24:25], -1, 0
	v_and_b32_e32 v129, 0x7e78, v185
	s_and_b64 s[24:25], s[14:15], s[24:25]
	v_mov_b32_e32 v128, 0
	v_mov_b32_e32 v132, 1.0
	v_lshlrev_b32_e32 v174, 2, v129
	v_mov_b32_e32 v134, 1.0
	v_mov_b32_e32 v135, 1.0
	v_mov_b32_e32 v136, 1.0
	v_mov_b32_e32 v137, 1.0
	v_mov_b32_e32 v138, 0
	v_mov_b32_e32 v139, 0
	v_mov_b32_e32 v140, 0
	v_mov_b32_e32 v141, 0
	v_mov_b32_e32 v142, 0
	v_mov_b32_e32 v143, 0
	v_mov_b32_e32 v144, 0
	v_mov_b32_e32 v145, 0
	v_mov_b32_e32 v146, 1.0
	v_mov_b32_e32 v147, 1.0
	v_mov_b32_e32 v148, 1.0
	v_mov_b32_e32 v149, 1.0
	s_and_saveexec_b64 s[26:27], s[24:25]
	s_cbranch_execz .LBB0_1827
	v_mov_b32_e32 v175, v159
	v_lshl_add_u64 v[238:239], v[162:163], 0, v[174:175]
	v_lshl_add_u64 v[236:237], v[160:161], 0, v[174:175]
	global_load_dwordx4 v[138:141], v[238:239], off offset:512
	global_load_dwordx4 v[142:145], v[238:239], off
	global_load_dwordx4 v[134:137], v[236:237], off offset:512
	global_load_dwordx4 v[146:149], v[236:237], off
	global_load_dwordx4 v[188:191], v[238:239], off offset:1536
	global_load_dwordx4 v[192:195], v[238:239], off offset:1024
	global_load_dwordx4 v[196:199], v[236:237], off offset:1536
	global_load_dwordx4 v[200:203], v[236:237], off offset:1024
	v_add_u32_e32 v240, 0x400, v185
	v_and_b32_e32 v240, 0x7e78, v240
	v_lshlrev_b32_e32 v240, 2, v240
	v_mov_b32_e32 v241, v159
	v_lshl_add_u64 v[238:239], v[162:163], 0, v[240:241]
	v_lshl_add_u64 v[236:237], v[160:161], 0, v[240:241]
	global_load_dwordx4 v[204:207], v[238:239], off offset:512
	global_load_dwordx4 v[208:211], v[238:239], off
	global_load_dwordx4 v[212:215], v[236:237], off offset:512
	global_load_dwordx4 v[216:219], v[236:237], off
	global_load_dwordx4 v[220:223], v[238:239], off offset:1536
	global_load_dwordx4 v[224:227], v[238:239], off offset:1024
	global_load_dwordx4 v[228:231], v[236:237], off offset:1536
	global_load_dwordx4 v[232:235], v[236:237], off offset:1024
	s_waitcnt vmcnt(12)
.LBB0_1827:
	s_or_b64 exec, exec, s[26:27]
	s_cmp_lt_u32 s28, 2
	s_cselect_b64 vcc, -1, 0
	s_lshl_b32 s19, s51, 2
	v_pk_mul_f32 v[186:187], v[120:121], v[142:143]
	v_pk_mul_f32 v[120:121], v[120:121], v[146:147]
	v_cndmask_b32_e32 v172, 1.0, v183, vcc
	s_and_b32 s19, s19, 4
	v_pk_mul_f32 v[130:131], v[122:123], v[144:145]
	v_pk_fma_f32 v[186:187], v[124:125], v[146:147], v[186:187] neg_lo:[0,0,1] neg_hi:[0,0,1]
	v_pk_fma_f32 v[120:121], v[124:125], v[142:143], v[120:121]
	s_or_b32 s28, s19, s47
	s_mul_i32 s19, s29, 3
	v_pk_fma_f32 v[130:131], v[126:127], v[148:149], v[130:131] neg_lo:[0,0,1] neg_hi:[0,0,1]
	v_pk_mul_f32 v[186:187], v[172:173], v[186:187] op_sel_hi:[0,1]
	v_pk_mul_f32 v[122:123], v[122:123], v[148:149]
	v_pk_mul_f32 v[120:121], v[172:173], v[120:121] op_sel_hi:[0,1]
	v_cvt_pk_bf16_f32 v124, v186, v187
	s_add_i32 s19, s19, s17
	v_pk_mul_f32 v[130:131], v[172:173], v[130:131] op_sel_hi:[0,1]
	v_pk_fma_f32 v[122:123], v[126:127], v[144:145], v[122:123]
	v_cvt_pk_bf16_f32 v125, v130, v131
	v_cvt_pk_bf16_f32 v126, v120, v121
	ds_bpermute_b32 v120, v179, v124
	s_lshl_b32 s29, s19, 7
	s_lshl_b32 s17, s17, 1
	s_sub_i32 s19, 12, s17
	v_pk_mul_f32 v[122:123], v[172:173], v[122:123] op_sel_hi:[0,1]
	v_cvt_pk_bf16_f32 v123, v122, v123
	ds_bpermute_b32 v121, v179, v125
	ds_bpermute_b32 v122, v179, v126
	ds_bpermute_b32 v123, v179, v123
	v_lshlrev_b32_e32 v242, s19, v178
	v_and_b32_e32 v242, 0xfff, v242
	v_lshrrev_b32_e32 v243, s17, v178
	v_add_lshl_u32 v242, v242, v243, 7
	v_add_u32_e32 v242, v242, v158
	s_lshr_b32 s101, s100, 12
	s_lshl_b32 s101, s101, 3
	s_add_i32 s101, s101, s29
	s_or_b32 s101, s101, s28
	s_lshl_b32 s101, s101, 19
	s_and_b32 s100, s100, 0xfff
	s_lshr_b32 s100, s100, s17
	s_lshl_b32 s100, s100, 7
	s_add_u32 s98, s6, s101
	s_addc_u32 s99, s7, 0
	s_add_u32 s98, s98, s2
	s_addc_u32 s99, s99, s3
	s_add_u32 s98, s98, s100
	s_addc_u32 s99, s99, 0
	s_mov_b64 s[100:101], s[98:99]
	s_waitcnt lgkmcnt(0)
	global_store_dwordx4 v242, v[120:123], s[100:101]
	s_nop 1
	s_or_b32 s30, s28, 2
	v_mov_b32_e32 v133, 1.0
	v_pk_mul_f32 v[122:123], v[112:113], v[142:143]
	v_pk_mul_f32 v[112:113], v[112:113], v[146:147]
	v_pk_mul_f32 v[120:121], v[114:115], v[144:145]
	v_pk_fma_f32 v[122:123], v[116:117], v[146:147], v[122:123] neg_lo:[0,0,1] neg_hi:[0,0,1]
	v_pk_mul_f32 v[114:115], v[114:115], v[148:149]
	v_pk_fma_f32 v[112:113], v[116:117], v[142:143], v[112:113]
	v_pk_fma_f32 v[120:121], v[118:119], v[148:149], v[120:121] neg_lo:[0,0,1] neg_hi:[0,0,1]
	v_pk_mul_f32 v[122:123], v[172:173], v[122:123] op_sel_hi:[0,1]
	v_pk_fma_f32 v[114:115], v[118:119], v[144:145], v[114:115]
	v_pk_mul_f32 v[112:113], v[172:173], v[112:113] op_sel_hi:[0,1]
	v_cvt_pk_bf16_f32 v116, v122, v123
	v_pk_mul_f32 v[120:121], v[172:173], v[120:121] op_sel_hi:[0,1]
	v_pk_mul_f32 v[114:115], v[172:173], v[114:115] op_sel_hi:[0,1]
	v_cvt_pk_bf16_f32 v117, v120, v121
	v_cvt_pk_bf16_f32 v118, v112, v113
	ds_bpermute_b32 v112, v179, v116
	v_cvt_pk_bf16_f32 v115, v114, v115
	ds_bpermute_b32 v113, v179, v117
	ds_bpermute_b32 v114, v179, v118
	ds_bpermute_b32 v115, v179, v115
	s_add_u32 s100, s98, 0x100000
	s_addc_u32 s101, s99, 0
	s_waitcnt lgkmcnt(0)
; __host__ __device__ __forceinline__ size_t qkv_block(int typ, int g, int b, int h) { return (size_t)((((typ * 3 + g) * 16 + b) * 8 + h)) * (4096 * 64); }
; __host__ __device__ __forceinline__ int qkv_row(int pos, int g) { const int dsh = 2 * g; return ((pos & ((1 << dsh) - 1)) << (12 - dsh)) + (pos >> dsh); }
; __device__ __forceinline__ u32x4 pack8(const f32x4 v0, const f32x4 v1) { u32x4 w; w.x = cvt_pk_bf16(v0[0], v0[1]); w.y = cvt_pk_bf16(v0[2], v0[3]); w.z = cvt_pk_bf16(v1[0], v1[1]); w.w = cvt_pk_bf16(v1[2], v1[3]); return w; }
;     __device__ __forceinline__ void operator()(const f32x4 (&acc)[2][2][4][2], const Unit& u, int wr, int wc, int fr, int fq) const {
;     ...
;             for (int mm = 0; mm < 2; ++mm) { const int pos = (row0 + ai * HALF + (2 * mp + mm) * 16) & (SEQ - 1);
;                 csv[mm] = *(const f32x4*)(rope + pos * 8 + 4 * (fq & 1)); snv[mm] = *(const f32x4*)(rope + 4096 * 8 + pos * 8 + 4 * (fq & 1)); }
; #pragma unroll
;             for (int mm = 0; mm < 2; ++mm) {
;                 const int m = 2 * mp + mm, row = row0 + ai * HALF + m * 16;
;                 f32x4 cs = {1.f, 1.f, 1.f, 1.f}, sn = {0.f, 0.f, 0.f, 0.f};
;                 if (rl) { cs = csv[mm]; sn = snv[mm]; }
; #pragma unroll
;                 for (int bj = 0; bj < 2; ++bj) {
;                     const f32x4 x1 = acc[ai][bj][m][0], x2 = acc[ai][bj][m][1];
;                     const f32x4 r1 = (x1 * cs - x2 * sn) * sc, r2 = (x2 * cs + x1 * sn) * sc;
;                     { const int tok = row_off + row - fr + tr_, hh = 4 * (u.pn & 1) + 2 * bj + (wc >> 1);
;                       *(u32x4*)(O + qkv_block(typ, gq_, tok >> 12, hh) + (size_t)qkv_row(tok & (SEQ - 1), gq_) * 64 + 32 * (wc & 1) + 8 * tq_) = xpose4x16(pack8(r1, r2), sa_); }
	global_store_dwordx4 v242, v[112:115], s[100:101]
	s_nop 1
	v_mov_b32_e32 v129, 0
	v_pk_mul_f32 v[114:115], v[104:105], v[138:139]
	v_pk_mul_f32 v[112:113], v[106:107], v[140:141]
	v_pk_fma_f32 v[114:115], v[108:109], v[134:135], v[114:115] neg_lo:[0,0,1] neg_hi:[0,0,1]
	v_pk_mul_f32 v[108:109], v[108:109], v[138:139]
	v_pk_fma_f32 v[112:113], v[110:111], v[136:137], v[112:113] neg_lo:[0,0,1] neg_hi:[0,0,1]
	v_pk_fma_f32 v[104:105], v[104:105], v[134:135], v[108:109]
	v_pk_mul_f32 v[114:115], v[172:173], v[114:115] op_sel_hi:[0,1]
	v_pk_mul_f32 v[110:111], v[110:111], v[140:141]
	v_pk_mul_f32 v[104:105], v[172:173], v[104:105] op_sel_hi:[0,1]
	v_cvt_pk_bf16_f32 v108, v114, v115
	v_pk_mul_f32 v[112:113], v[172:173], v[112:113] op_sel_hi:[0,1]
	v_pk_fma_f32 v[106:107], v[106:107], v[136:137], v[110:111]
	v_cvt_pk_bf16_f32 v109, v112, v113
	v_cvt_pk_bf16_f32 v110, v104, v105
	ds_bpermute_b32 v104, v179, v108
	v_pk_mul_f32 v[106:107], v[172:173], v[106:107] op_sel_hi:[0,1]
	v_cvt_pk_bf16_f32 v107, v106, v107
	ds_bpermute_b32 v105, v179, v109
	ds_bpermute_b32 v106, v179, v110
	ds_bpermute_b32 v107, v179, v107
	s_lshr_b32 s100, 0x800, s17
	s_add_u32 s100, s98, s100
	s_addc_u32 s101, s99, 0
	s_waitcnt lgkmcnt(0)
	global_store_dwordx4 v242, v[104:107], s[100:101]
	s_nop 1
	v_mov_b32_e32 v130, 0
	v_mov_b32_e32 v131, 0
	v_pk_mul_f32 v[106:107], v[96:97], v[138:139]
	v_pk_mul_f32 v[104:105], v[98:99], v[140:141]
	v_pk_fma_f32 v[106:107], v[100:101], v[134:135], v[106:107] neg_lo:[0,0,1] neg_hi:[0,0,1]
	v_pk_mul_f32 v[100:101], v[100:101], v[138:139]
	v_pk_fma_f32 v[104:105], v[102:103], v[136:137], v[104:105] neg_lo:[0,0,1] neg_hi:[0,0,1]
	v_pk_mul_f32 v[102:103], v[102:103], v[140:141]
	v_pk_fma_f32 v[96:97], v[96:97], v[134:135], v[100:101]
	v_pk_mul_f32 v[106:107], v[172:173], v[106:107] op_sel_hi:[0,1]
	v_pk_fma_f32 v[98:99], v[98:99], v[136:137], v[102:103]
	v_pk_mul_f32 v[96:97], v[172:173], v[96:97] op_sel_hi:[0,1]
	v_cvt_pk_bf16_f32 v100, v106, v107
	v_pk_mul_f32 v[104:105], v[172:173], v[104:105] op_sel_hi:[0,1]
	v_pk_mul_f32 v[98:99], v[172:173], v[98:99] op_sel_hi:[0,1]
	v_cvt_pk_bf16_f32 v101, v104, v105
	v_cvt_pk_bf16_f32 v102, v96, v97
	ds_bpermute_b32 v96, v179, v100
	v_cvt_pk_bf16_f32 v99, v98, v99
	ds_bpermute_b32 v97, v179, v101
	ds_bpermute_b32 v98, v179, v102
	ds_bpermute_b32 v99, v179, v99
	s_lshr_b32 s100, 0x800, s17
	s_add_i32 s100, s100, 0x100000
	s_add_u32 s100, s98, s100
	s_addc_u32 s101, s99, 0
	s_waitcnt lgkmcnt(0)
	global_store_dwordx4 v242, v[96:99], s[100:101]
	s_nop 1
	v_mov_b32_e32 v134, 1.0
	v_mov_b32_e32 v135, 1.0
	v_mov_b32_e32 v96, 0
	v_mov_b32_e32 v97, 0
	v_mov_b32_e32 v98, 0
	v_mov_b32_e32 v99, 0
	v_mov_b32_e32 v100, 1.0
	v_mov_b32_e32 v101, 1.0
	v_mov_b32_e32 v102, 1.0
	v_mov_b32_e32 v103, 1.0
	s_and_saveexec_b64 s[26:27], s[24:25]
	s_cbranch_execz .LBB0_1829
	s_waitcnt vmcnt(12)
	v_mov_b64_e32 v[128:129], v[188:189]
	v_mov_b64_e32 v[130:131], v[190:191]
	v_mov_b64_e32 v[96:97], v[192:193]
	v_mov_b64_e32 v[98:99], v[194:195]
	v_mov_b64_e32 v[132:133], v[196:197]
	v_mov_b64_e32 v[134:135], v[198:199]
	v_mov_b64_e32 v[100:101], v[200:201]
	v_mov_b64_e32 v[102:103], v[202:203]
.LBB0_1829:
	s_or_b64 exec, exec, s[26:27]
	v_pk_mul_f32 v[106:107], v[88:89], v[96:97]
	v_pk_mul_f32 v[88:89], v[88:89], v[100:101]
	v_mov_b32_e32 v173, v172
	v_pk_mul_f32 v[104:105], v[90:91], v[98:99]
	v_pk_fma_f32 v[106:107], v[92:93], v[100:101], v[106:107] neg_lo:[0,0,1] neg_hi:[0,0,1]
	v_pk_fma_f32 v[88:89], v[92:93], v[96:97], v[88:89]
	v_pk_fma_f32 v[108:109], v[94:95], v[102:103], v[104:105] neg_lo:[0,0,1] neg_hi:[0,0,1]
	v_mov_b32_e32 v104, v172
	v_mov_b32_e32 v105, v172
	v_pk_mul_f32 v[106:107], v[172:173], v[106:107]
	v_pk_mul_f32 v[90:91], v[90:91], v[102:103]
	v_pk_mul_f32 v[88:89], v[172:173], v[88:89]
	v_cvt_pk_bf16_f32 v92, v106, v107
	v_pk_mul_f32 v[108:109], v[104:105], v[108:109]
	v_pk_fma_f32 v[90:91], v[94:95], v[98:99], v[90:91]
	v_cvt_pk_bf16_f32 v93, v108, v109
	v_cvt_pk_bf16_f32 v94, v88, v89
	ds_bpermute_b32 v88, v179, v92
	v_pk_mul_f32 v[90:91], v[104:105], v[90:91]
	v_cvt_pk_bf16_f32 v91, v90, v91
	ds_bpermute_b32 v89, v179, v93
	ds_bpermute_b32 v90, v179, v94
	ds_bpermute_b32 v91, v179, v91
	s_lshr_b32 s100, 0x1000, s17
	s_add_u32 s100, s98, s100
	s_addc_u32 s101, s99, 0
	s_waitcnt lgkmcnt(0)
	global_store_dwordx4 v242, v[88:91], s[100:101]
	s_nop 1
	v_pk_mul_f32 v[90:91], v[80:81], v[96:97]
	v_pk_mul_f32 v[80:81], v[80:81], v[100:101]
	v_pk_mul_f32 v[88:89], v[82:83], v[98:99]
	v_pk_fma_f32 v[90:91], v[84:85], v[100:101], v[90:91] neg_lo:[0,0,1] neg_hi:[0,0,1]
	v_pk_mul_f32 v[82:83], v[82:83], v[102:103]
	v_pk_fma_f32 v[80:81], v[84:85], v[96:97], v[80:81]
	v_pk_fma_f32 v[88:89], v[86:87], v[102:103], v[88:89] neg_lo:[0,0,1] neg_hi:[0,0,1]
	v_pk_mul_f32 v[90:91], v[172:173], v[90:91]
	v_pk_fma_f32 v[82:83], v[86:87], v[98:99], v[82:83]
	v_pk_mul_f32 v[80:81], v[172:173], v[80:81]
	v_cvt_pk_bf16_f32 v84, v90, v91
	v_pk_mul_f32 v[88:89], v[104:105], v[88:89]
	v_pk_mul_f32 v[82:83], v[104:105], v[82:83]
	v_cvt_pk_bf16_f32 v85, v88, v89
	v_cvt_pk_bf16_f32 v86, v80, v81
	ds_bpermute_b32 v80, v179, v84
	v_cvt_pk_bf16_f32 v83, v82, v83
	ds_bpermute_b32 v81, v179, v85
	ds_bpermute_b32 v82, v179, v86
	ds_bpermute_b32 v83, v179, v83
	s_lshr_b32 s100, 0x1000, s17
	s_add_i32 s100, s100, 0x100000
	s_add_u32 s100, s98, s100
	s_addc_u32 s101, s99, 0
	s_waitcnt lgkmcnt(0)
; __host__ __device__ __forceinline__ size_t qkv_block(int typ, int g, int b, int h) { return (size_t)((((typ * 3 + g) * 16 + b) * 8 + h)) * (4096 * 64); }
; __host__ __device__ __forceinline__ int qkv_row(int pos, int g) { const int dsh = 2 * g; return ((pos & ((1 << dsh) - 1)) << (12 - dsh)) + (pos >> dsh); }
; __device__ __forceinline__ u32x4 pack8(const f32x4 v0, const f32x4 v1) { u32x4 w; w.x = cvt_pk_bf16(v0[0], v0[1]); w.y = cvt_pk_bf16(v0[2], v0[3]); w.z = cvt_pk_bf16(v1[0], v1[1]); w.w = cvt_pk_bf16(v1[2], v1[3]); return w; }
;     __device__ __forceinline__ void operator()(const f32x4 (&acc)[2][2][4][2], const Unit& u, int wr, int wc, int fr, int fq) const {
;     ...
;             for (int mm = 0; mm < 2; ++mm) { const int pos = (row0 + ai * HALF + (2 * mp + mm) * 16) & (SEQ - 1);
;                 csv[mm] = *(const f32x4*)(rope + pos * 8 + 4 * (fq & 1)); snv[mm] = *(const f32x4*)(rope + 4096 * 8 + pos * 8 + 4 * (fq & 1)); }
; #pragma unroll
;             for (int mm = 0; mm < 2; ++mm) {
;                 const int m = 2 * mp + mm, row = row0 + ai * HALF + m * 16;
;                 f32x4 cs = {1.f, 1.f, 1.f, 1.f}, sn = {0.f, 0.f, 0.f, 0.f};
;                 if (rl) { cs = csv[mm]; sn = snv[mm]; }
; #pragma unroll
;                 for (int bj = 0; bj < 2; ++bj) {
;                     const f32x4 x1 = acc[ai][bj][m][0], x2 = acc[ai][bj][m][1];
;                     const f32x4 r1 = (x1 * cs - x2 * sn) * sc, r2 = (x2 * cs + x1 * sn) * sc;
;                     { const int tok = row_off + row - fr + tr_, hh = 4 * (u.pn & 1) + 2 * bj + (wc >> 1);
;                       *(u32x4*)(O + qkv_block(typ, gq_, tok >> 12, hh) + (size_t)qkv_row(tok & (SEQ - 1), gq_) * 64 + 32 * (wc & 1) + 8 * tq_) = xpose4x16(pack8(r1, r2), sa_); }
	global_store_dwordx4 v242, v[80:83], s[100:101]
	s_nop 1
	v_mov_b32_e32 v85, 1.0
	v_pk_mul_f32 v[82:83], v[72:73], v[128:129]
	v_pk_mul_f32 v[80:81], v[74:75], v[130:131]
	v_pk_fma_f32 v[82:83], v[76:77], v[132:133], v[82:83] neg_lo:[0,0,1] neg_hi:[0,0,1]
	v_pk_mul_f32 v[76:77], v[76:77], v[128:129]
	v_pk_fma_f32 v[80:81], v[78:79], v[134:135], v[80:81] neg_lo:[0,0,1] neg_hi:[0,0,1]
	v_pk_fma_f32 v[72:73], v[72:73], v[132:133], v[76:77]
	v_pk_mul_f32 v[82:83], v[172:173], v[82:83]
	v_pk_mul_f32 v[78:79], v[78:79], v[130:131]
	v_pk_mul_f32 v[72:73], v[172:173], v[72:73]
	v_cvt_pk_bf16_f32 v76, v82, v83
	v_pk_mul_f32 v[80:81], v[104:105], v[80:81]
	v_pk_fma_f32 v[74:75], v[74:75], v[134:135], v[78:79]
	v_cvt_pk_bf16_f32 v77, v80, v81
	v_cvt_pk_bf16_f32 v78, v72, v73
	ds_bpermute_b32 v72, v179, v76
	v_pk_mul_f32 v[74:75], v[104:105], v[74:75]
	v_cvt_pk_bf16_f32 v75, v74, v75
	ds_bpermute_b32 v73, v179, v77
	ds_bpermute_b32 v74, v179, v78
	ds_bpermute_b32 v75, v179, v75
	s_lshr_b32 s100, 0x1800, s17
	s_add_u32 s100, s98, s100
	s_addc_u32 s101, s99, 0
	s_waitcnt lgkmcnt(0)
	global_store_dwordx4 v242, v[72:75], s[100:101]
	s_nop 1
	v_mov_b32_e32 v76, 0
	v_mov_b32_e32 v77, 0
	v_pk_mul_f32 v[74:75], v[64:65], v[128:129]
	v_pk_mul_f32 v[72:73], v[66:67], v[130:131]
	v_pk_fma_f32 v[74:75], v[68:69], v[132:133], v[74:75] neg_lo:[0,0,1] neg_hi:[0,0,1]
	v_pk_mul_f32 v[68:69], v[68:69], v[128:129]
	v_pk_fma_f32 v[72:73], v[70:71], v[134:135], v[72:73] neg_lo:[0,0,1] neg_hi:[0,0,1]
	v_pk_mul_f32 v[70:71], v[70:71], v[130:131]
	v_pk_fma_f32 v[64:65], v[64:65], v[132:133], v[68:69]
	v_pk_mul_f32 v[74:75], v[172:173], v[74:75]
	v_pk_fma_f32 v[66:67], v[66:67], v[134:135], v[70:71]
	v_pk_mul_f32 v[64:65], v[172:173], v[64:65]
	v_cvt_pk_bf16_f32 v68, v74, v75
	v_pk_mul_f32 v[72:73], v[104:105], v[72:73]
	v_pk_mul_f32 v[66:67], v[104:105], v[66:67]
	v_cvt_pk_bf16_f32 v69, v72, v73
	v_cvt_pk_bf16_f32 v70, v64, v65
	ds_bpermute_b32 v64, v179, v68
	v_cvt_pk_bf16_f32 v67, v66, v67
	ds_bpermute_b32 v65, v179, v69
	ds_bpermute_b32 v66, v179, v70
	ds_bpermute_b32 v67, v179, v67
	s_lshr_b32 s100, 0x1800, s17
	s_add_i32 s100, s100, 0x100000
	s_add_u32 s100, s98, s100
	s_addc_u32 s101, s99, 0
	s_waitcnt lgkmcnt(0)
	global_store_dwordx4 v242, v[64:67], s[100:101]
	s_nop 1
	v_mov_b32_e32 v68, 1.0
	v_mov_b32_e32 v70, 1.0
	v_add_u32_e32 v64, 0x400, v185
	v_and_b32_e32 v65, 0x7e78, v64
	v_mov_b32_e32 v64, 0
	v_lshlrev_b32_e32 v86, 2, v65
	v_mov_b32_e32 v71, 1.0
	v_mov_b32_e32 v72, 1.0
	v_mov_b32_e32 v73, 1.0
	v_mov_b32_e32 v74, 0
	v_mov_b32_e32 v75, 0
	v_mov_b32_e32 v78, 0
	v_mov_b32_e32 v79, 0
	v_mov_b32_e32 v80, 0
	v_mov_b32_e32 v81, 0
	v_mov_b32_e32 v82, 1.0
	v_mov_b32_e32 v83, 1.0
	v_mov_b32_e32 v84, 1.0
	s_and_saveexec_b64 s[26:27], s[24:25]
	s_cbranch_execz .LBB0_1831
	s_waitcnt vmcnt(12)
	v_mov_b64_e32 v[74:75], v[204:205]
	v_mov_b64_e32 v[76:77], v[206:207]
	v_mov_b64_e32 v[78:79], v[208:209]
	v_mov_b64_e32 v[80:81], v[210:211]
	v_mov_b64_e32 v[70:71], v[212:213]
	v_mov_b64_e32 v[72:73], v[214:215]
	v_mov_b64_e32 v[82:83], v[216:217]
	v_mov_b64_e32 v[84:85], v[218:219]
.LBB0_1831:
	s_or_b64 exec, exec, s[26:27]
	v_pk_mul_f32 v[88:89], v[56:57], v[78:79]
	v_pk_mul_f32 v[56:57], v[56:57], v[82:83]
	v_pk_mul_f32 v[66:67], v[58:59], v[80:81]
	v_pk_fma_f32 v[88:89], v[60:61], v[82:83], v[88:89] neg_lo:[0,0,1] neg_hi:[0,0,1]
	v_pk_fma_f32 v[56:57], v[60:61], v[78:79], v[56:57]
	v_pk_fma_f32 v[66:67], v[62:63], v[84:85], v[66:67] neg_lo:[0,0,1] neg_hi:[0,0,1]
	v_pk_mul_f32 v[88:89], v[172:173], v[88:89]
	v_pk_mul_f32 v[58:59], v[58:59], v[84:85]
	v_pk_mul_f32 v[56:57], v[172:173], v[56:57]
	v_cvt_pk_bf16_f32 v60, v88, v89
	v_pk_mul_f32 v[66:67], v[104:105], v[66:67]
	v_pk_fma_f32 v[58:59], v[62:63], v[80:81], v[58:59]
	v_cvt_pk_bf16_f32 v61, v66, v67
	v_cvt_pk_bf16_f32 v62, v56, v57
	ds_bpermute_b32 v56, v179, v60
	v_pk_mul_f32 v[58:59], v[104:105], v[58:59]
	v_cvt_pk_bf16_f32 v59, v58, v59
	ds_bpermute_b32 v57, v179, v61
	ds_bpermute_b32 v58, v179, v62
	ds_bpermute_b32 v59, v179, v59
	s_lshr_b32 s100, 0x4000, s17
	s_add_u32 s100, s98, s100
	s_addc_u32 s101, s99, 0
	s_waitcnt lgkmcnt(0)
	global_store_dwordx4 v242, v[56:59], s[100:101]
	s_nop 1
	v_mov_b32_e32 v69, 1.0
	v_mov_b32_e32 v65, 0
	v_pk_mul_f32 v[58:59], v[48:49], v[78:79]
	v_pk_mul_f32 v[48:49], v[48:49], v[82:83]
	v_pk_mul_f32 v[56:57], v[50:51], v[80:81]
	v_pk_fma_f32 v[58:59], v[52:53], v[82:83], v[58:59] neg_lo:[0,0,1] neg_hi:[0,0,1]
	v_pk_mul_f32 v[50:51], v[50:51], v[84:85]
	v_pk_fma_f32 v[48:49], v[52:53], v[78:79], v[48:49]
	v_pk_fma_f32 v[56:57], v[54:55], v[84:85], v[56:57] neg_lo:[0,0,1] neg_hi:[0,0,1]
	v_pk_mul_f32 v[58:59], v[172:173], v[58:59]
	v_pk_fma_f32 v[50:51], v[54:55], v[80:81], v[50:51]
	v_pk_mul_f32 v[48:49], v[172:173], v[48:49]
	v_cvt_pk_bf16_f32 v52, v58, v59
	v_pk_mul_f32 v[56:57], v[104:105], v[56:57]
	v_pk_mul_f32 v[50:51], v[104:105], v[50:51]
	v_cvt_pk_bf16_f32 v53, v56, v57
	v_cvt_pk_bf16_f32 v54, v48, v49
	ds_bpermute_b32 v48, v179, v52
	v_cvt_pk_bf16_f32 v51, v50, v51
	ds_bpermute_b32 v49, v179, v53
	ds_bpermute_b32 v50, v179, v54
	ds_bpermute_b32 v51, v179, v51
	s_lshr_b32 s100, 0x4000, s17
	s_add_i32 s100, s100, 0x100000
	s_add_u32 s100, s98, s100
	s_addc_u32 s101, s99, 0
	s_waitcnt lgkmcnt(0)
; __host__ __device__ __forceinline__ size_t qkv_block(int typ, int g, int b, int h) { return (size_t)((((typ * 3 + g) * 16 + b) * 8 + h)) * (4096 * 64); }
; __host__ __device__ __forceinline__ int qkv_row(int pos, int g) { const int dsh = 2 * g; return ((pos & ((1 << dsh) - 1)) << (12 - dsh)) + (pos >> dsh); }
; __device__ __forceinline__ u32x4 pack8(const f32x4 v0, const f32x4 v1) { u32x4 w; w.x = cvt_pk_bf16(v0[0], v0[1]); w.y = cvt_pk_bf16(v0[2], v0[3]); w.z = cvt_pk_bf16(v1[0], v1[1]); w.w = cvt_pk_bf16(v1[2], v1[3]); return w; }
;     __device__ __forceinline__ void operator()(const f32x4 (&acc)[2][2][4][2], const Unit& u, int wr, int wc, int fr, int fq) const {
;     ...
;             for (int mm = 0; mm < 2; ++mm) { const int pos = (row0 + ai * HALF + (2 * mp + mm) * 16) & (SEQ - 1);
;                 csv[mm] = *(const f32x4*)(rope + pos * 8 + 4 * (fq & 1)); snv[mm] = *(const f32x4*)(rope + 4096 * 8 + pos * 8 + 4 * (fq & 1)); }
; #pragma unroll
;             for (int mm = 0; mm < 2; ++mm) {
;                 const int m = 2 * mp + mm, row = row0 + ai * HALF + m * 16;
;                 f32x4 cs = {1.f, 1.f, 1.f, 1.f}, sn = {0.f, 0.f, 0.f, 0.f};
;                 if (rl) { cs = csv[mm]; sn = snv[mm]; }
; #pragma unroll
;                 for (int bj = 0; bj < 2; ++bj) {
;                     const f32x4 x1 = acc[ai][bj][m][0], x2 = acc[ai][bj][m][1];
;                     const f32x4 r1 = (x1 * cs - x2 * sn) * sc, r2 = (x2 * cs + x1 * sn) * sc;
;                     { const int tok = row_off + row - fr + tr_, hh = 4 * (u.pn & 1) + 2 * bj + (wc >> 1);
;                       *(u32x4*)(O + qkv_block(typ, gq_, tok >> 12, hh) + (size_t)qkv_row(tok & (SEQ - 1), gq_) * 64 + 32 * (wc & 1) + 8 * tq_) = xpose4x16(pack8(r1, r2), sa_); }
	global_store_dwordx4 v242, v[48:51], s[100:101]
	s_nop 1
	v_mov_b32_e32 v66, 0
	v_pk_mul_f32 v[50:51], v[40:41], v[74:75]
	v_pk_mul_f32 v[48:49], v[42:43], v[76:77]
	v_pk_fma_f32 v[50:51], v[44:45], v[70:71], v[50:51] neg_lo:[0,0,1] neg_hi:[0,0,1]
	v_pk_mul_f32 v[44:45], v[44:45], v[74:75]
	v_pk_fma_f32 v[48:49], v[46:47], v[72:73], v[48:49] neg_lo:[0,0,1] neg_hi:[0,0,1]
	v_pk_fma_f32 v[40:41], v[40:41], v[70:71], v[44:45]
	v_pk_mul_f32 v[50:51], v[172:173], v[50:51]
	v_pk_mul_f32 v[46:47], v[46:47], v[76:77]
	v_pk_mul_f32 v[40:41], v[172:173], v[40:41]
	v_cvt_pk_bf16_f32 v44, v50, v51
	v_pk_mul_f32 v[48:49], v[104:105], v[48:49]
	v_pk_fma_f32 v[42:43], v[42:43], v[72:73], v[46:47]
	v_cvt_pk_bf16_f32 v45, v48, v49
	v_cvt_pk_bf16_f32 v46, v40, v41
	ds_bpermute_b32 v40, v179, v44
	v_pk_mul_f32 v[42:43], v[104:105], v[42:43]
	v_cvt_pk_bf16_f32 v43, v42, v43
	ds_bpermute_b32 v41, v179, v45
	ds_bpermute_b32 v42, v179, v46
	ds_bpermute_b32 v43, v179, v43
	s_lshr_b32 s100, 0x4800, s17
	s_add_u32 s100, s98, s100
	s_addc_u32 s101, s99, 0
	s_waitcnt lgkmcnt(0)
	global_store_dwordx4 v242, v[40:43], s[100:101]
	s_nop 1
	v_mov_b32_e32 v67, 0
	s_nop 0
	v_pk_mul_f32 v[42:43], v[32:33], v[74:75]
	v_pk_mul_f32 v[40:41], v[34:35], v[76:77]
	v_pk_fma_f32 v[42:43], v[36:37], v[70:71], v[42:43] neg_lo:[0,0,1] neg_hi:[0,0,1]
	v_pk_mul_f32 v[36:37], v[36:37], v[74:75]
	v_pk_fma_f32 v[40:41], v[38:39], v[72:73], v[40:41] neg_lo:[0,0,1] neg_hi:[0,0,1]
	v_pk_mul_f32 v[38:39], v[38:39], v[76:77]
	v_pk_fma_f32 v[32:33], v[32:33], v[70:71], v[36:37]
	v_pk_mul_f32 v[42:43], v[172:173], v[42:43]
	v_pk_fma_f32 v[34:35], v[34:35], v[72:73], v[38:39]
	v_pk_mul_f32 v[32:33], v[172:173], v[32:33]
	v_cvt_pk_bf16_f32 v36, v42, v43
	v_pk_mul_f32 v[40:41], v[104:105], v[40:41]
	v_pk_mul_f32 v[34:35], v[104:105], v[34:35]
	v_cvt_pk_bf16_f32 v37, v40, v41
	v_cvt_pk_bf16_f32 v38, v32, v33
	ds_bpermute_b32 v32, v179, v36
	v_cvt_pk_bf16_f32 v35, v34, v35
	ds_bpermute_b32 v33, v179, v37
	ds_bpermute_b32 v34, v179, v38
	ds_bpermute_b32 v35, v179, v35
	s_lshr_b32 s100, 0x4800, s17
	s_add_i32 s100, s100, 0x100000
	s_add_u32 s100, s98, s100
	s_addc_u32 s101, s99, 0
	s_waitcnt lgkmcnt(0)
	global_store_dwordx4 v242, v[32:35], s[100:101]
	s_nop 1
	v_mov_b32_e32 v70, 1.0
	v_mov_b32_e32 v71, 1.0
	v_mov_b32_e32 v32, 0
	v_mov_b32_e32 v33, 0
	v_mov_b32_e32 v34, 0
	v_mov_b32_e32 v35, 0
	v_mov_b32_e32 v36, 1.0
	v_mov_b32_e32 v37, 1.0
	v_mov_b32_e32 v38, 1.0
	v_mov_b32_e32 v39, 1.0
	s_and_saveexec_b64 s[26:27], s[24:25]
	s_cbranch_execz .LBB0_1833
	s_waitcnt vmcnt(12)
	v_mov_b64_e32 v[64:65], v[220:221]
	v_mov_b64_e32 v[66:67], v[222:223]
	v_mov_b64_e32 v[32:33], v[224:225]
	v_mov_b64_e32 v[34:35], v[226:227]
	v_mov_b64_e32 v[68:69], v[228:229]
	v_mov_b64_e32 v[70:71], v[230:231]
	v_mov_b64_e32 v[36:37], v[232:233]
	v_mov_b64_e32 v[38:39], v[234:235]
; __host__ __device__ __forceinline__ size_t qkv_block(int typ, int g, int b, int h) { return (size_t)((((typ * 3 + g) * 16 + b) * 8 + h)) * (4096 * 64); }
; __host__ __device__ __forceinline__ int qkv_row(int pos, int g) { const int dsh = 2 * g; return ((pos & ((1 << dsh) - 1)) << (12 - dsh)) + (pos >> dsh); }
; __device__ __forceinline__ u32x4 pack8(const f32x4 v0, const f32x4 v1) { u32x4 w; w.x = cvt_pk_bf16(v0[0], v0[1]); w.y = cvt_pk_bf16(v0[2], v0[3]); w.z = cvt_pk_bf16(v1[0], v1[1]); w.w = cvt_pk_bf16(v1[2], v1[3]); return w; }
;     __device__ __forceinline__ void operator()(const f32x4 (&acc)[2][2][4][2], const Unit& u, int wr, int wc, int fr, int fq) const {
;     ...
;             for (int mm = 0; mm < 2; ++mm) { const int pos = (row0 + ai * HALF + (2 * mp + mm) * 16) & (SEQ - 1);
;                 csv[mm] = *(const f32x4*)(rope + pos * 8 + 4 * (fq & 1)); snv[mm] = *(const f32x4*)(rope + 4096 * 8 + pos * 8 + 4 * (fq & 1)); }
; #pragma unroll
;             for (int mm = 0; mm < 2; ++mm) {
;                 const int m = 2 * mp + mm, row = row0 + ai * HALF + m * 16;
;                 f32x4 cs = {1.f, 1.f, 1.f, 1.f}, sn = {0.f, 0.f, 0.f, 0.f};
;                 if (rl) { cs = csv[mm]; sn = snv[mm]; }
; #pragma unroll
;                 for (int bj = 0; bj < 2; ++bj) {
;                     const f32x4 x1 = acc[ai][bj][m][0], x2 = acc[ai][bj][m][1];
;                     const f32x4 r1 = (x1 * cs - x2 * sn) * sc, r2 = (x2 * cs + x1 * sn) * sc;
;                     { const int tok = row_off + row - fr + tr_, hh = 4 * (u.pn & 1) + 2 * bj + (wc >> 1);
;                       *(u32x4*)(O + qkv_block(typ, gq_, tok >> 12, hh) + (size_t)qkv_row(tok & (SEQ - 1), gq_) * 64 + 32 * (wc & 1) + 8 * tq_) = xpose4x16(pack8(r1, r2), sa_); }
.LBB0_1833:
	s_or_b64 exec, exec, s[26:27]
	v_pk_mul_f32 v[42:43], v[24:25], v[32:33]
	v_pk_mul_f32 v[24:25], v[24:25], v[36:37]
	v_pk_mul_f32 v[40:41], v[26:27], v[34:35]
	v_pk_fma_f32 v[42:43], v[28:29], v[36:37], v[42:43] neg_lo:[0,0,1] neg_hi:[0,0,1]
	v_pk_fma_f32 v[24:25], v[28:29], v[32:33], v[24:25]
	v_pk_fma_f32 v[40:41], v[30:31], v[38:39], v[40:41] neg_lo:[0,0,1] neg_hi:[0,0,1]
	v_mov_b32_e32 v44, v172
	v_mov_b32_e32 v45, v172
	v_pk_mul_f32 v[42:43], v[172:173], v[42:43]
	v_pk_mul_f32 v[26:27], v[26:27], v[38:39]
	v_pk_mul_f32 v[24:25], v[172:173], v[24:25]
	v_cvt_pk_bf16_f32 v28, v42, v43
	v_pk_mul_f32 v[40:41], v[44:45], v[40:41]
	v_pk_fma_f32 v[26:27], v[30:31], v[34:35], v[26:27]
	v_cvt_pk_bf16_f32 v29, v40, v41
	v_cvt_pk_bf16_f32 v30, v24, v25
	ds_bpermute_b32 v24, v179, v28
	v_pk_mul_f32 v[26:27], v[44:45], v[26:27]
	v_cvt_pk_bf16_f32 v27, v26, v27
	ds_bpermute_b32 v25, v179, v29
	ds_bpermute_b32 v26, v179, v30
	ds_bpermute_b32 v27, v179, v27
	s_lshr_b32 s100, 0x5000, s17
	s_add_u32 s100, s98, s100
	s_addc_u32 s101, s99, 0
	s_waitcnt lgkmcnt(0)
	global_store_dwordx4 v242, v[24:27], s[100:101]
	s_nop 1
	s_andn2_b64 vcc, exec, s[0:1]
	s_mov_b64 s[0:1], -1
	v_pk_mul_f32 v[26:27], v[16:17], v[32:33]
	v_pk_mul_f32 v[16:17], v[16:17], v[36:37]
	v_pk_mul_f32 v[24:25], v[18:19], v[34:35]
	v_pk_fma_f32 v[26:27], v[20:21], v[36:37], v[26:27] neg_lo:[0,0,1] neg_hi:[0,0,1]
	v_pk_mul_f32 v[18:19], v[18:19], v[38:39]
	v_pk_fma_f32 v[16:17], v[20:21], v[32:33], v[16:17]
	v_pk_fma_f32 v[24:25], v[22:23], v[38:39], v[24:25] neg_lo:[0,0,1] neg_hi:[0,0,1]
	v_pk_mul_f32 v[26:27], v[172:173], v[26:27]
	v_pk_fma_f32 v[18:19], v[22:23], v[34:35], v[18:19]
	v_pk_mul_f32 v[16:17], v[172:173], v[16:17]
	v_cvt_pk_bf16_f32 v20, v26, v27
	v_pk_mul_f32 v[24:25], v[44:45], v[24:25]
	v_pk_mul_f32 v[18:19], v[44:45], v[18:19]
	v_cvt_pk_bf16_f32 v21, v24, v25
	v_cvt_pk_bf16_f32 v22, v16, v17
	ds_bpermute_b32 v16, v179, v20
	v_cvt_pk_bf16_f32 v19, v18, v19
	ds_bpermute_b32 v17, v179, v21
	ds_bpermute_b32 v18, v179, v22
	ds_bpermute_b32 v19, v179, v19
	s_lshr_b32 s100, 0x5000, s17
	s_add_i32 s100, s100, 0x100000
	s_add_u32 s100, s98, s100
	s_addc_u32 s101, s99, 0
	s_waitcnt lgkmcnt(0)
	global_store_dwordx4 v242, v[16:19], s[100:101]
	s_nop 1
	s_nop 0
	v_pk_mul_f32 v[18:19], v[8:9], v[64:65]
	v_pk_mul_f32 v[16:17], v[10:11], v[66:67]
	v_pk_fma_f32 v[18:19], v[12:13], v[68:69], v[18:19] neg_lo:[0,0,1] neg_hi:[0,0,1]
	v_pk_mul_f32 v[12:13], v[12:13], v[64:65]
	v_pk_fma_f32 v[16:17], v[14:15], v[70:71], v[16:17] neg_lo:[0,0,1] neg_hi:[0,0,1]
	v_pk_fma_f32 v[8:9], v[8:9], v[68:69], v[12:13]
	v_pk_mul_f32 v[18:19], v[172:173], v[18:19]
	v_pk_mul_f32 v[14:15], v[14:15], v[66:67]
	v_pk_mul_f32 v[8:9], v[172:173], v[8:9]
	v_cvt_pk_bf16_f32 v12, v18, v19
	v_pk_mul_f32 v[16:17], v[44:45], v[16:17]
	v_pk_fma_f32 v[10:11], v[10:11], v[70:71], v[14:15]
	v_cvt_pk_bf16_f32 v13, v16, v17
	v_cvt_pk_bf16_f32 v14, v8, v9
	ds_bpermute_b32 v8, v179, v12
	v_pk_mul_f32 v[10:11], v[44:45], v[10:11]
	v_cvt_pk_bf16_f32 v11, v10, v11
	ds_bpermute_b32 v9, v179, v13
	ds_bpermute_b32 v10, v179, v14
	ds_bpermute_b32 v11, v179, v11
	s_lshr_b32 s100, 0x5800, s17
	s_add_u32 s100, s98, s100
	s_addc_u32 s101, s99, 0
	s_waitcnt lgkmcnt(0)
	global_store_dwordx4 v242, v[8:11], s[100:101]
	s_nop 1
	v_pk_mul_f32 v[10:11], v[0:1], v[64:65]
	v_pk_mul_f32 v[8:9], v[2:3], v[66:67]
	v_pk_fma_f32 v[10:11], v[4:5], v[68:69], v[10:11] neg_lo:[0,0,1] neg_hi:[0,0,1]
	v_pk_mul_f32 v[4:5], v[4:5], v[64:65]
	v_pk_fma_f32 v[8:9], v[6:7], v[70:71], v[8:9] neg_lo:[0,0,1] neg_hi:[0,0,1]
	v_pk_mul_f32 v[6:7], v[6:7], v[66:67]
	v_pk_fma_f32 v[0:1], v[0:1], v[68:69], v[4:5]
	v_pk_mul_f32 v[10:11], v[172:173], v[10:11]
	v_pk_fma_f32 v[2:3], v[2:3], v[70:71], v[6:7]
	v_pk_mul_f32 v[0:1], v[172:173], v[0:1]
	v_cvt_pk_bf16_f32 v4, v10, v11
	v_pk_mul_f32 v[8:9], v[44:45], v[8:9]
	v_pk_mul_f32 v[2:3], v[44:45], v[2:3]
	v_cvt_pk_bf16_f32 v5, v8, v9
	v_cvt_pk_bf16_f32 v6, v0, v1
	ds_bpermute_b32 v0, v179, v4
	v_cvt_pk_bf16_f32 v3, v2, v3
	ds_bpermute_b32 v1, v179, v5
	ds_bpermute_b32 v2, v179, v6
	ds_bpermute_b32 v3, v179, v3
	s_lshr_b32 s100, 0x5800, s17
	s_add_i32 s100, s100, 0x100000
	s_add_u32 s100, s98, s100
	s_addc_u32 s101, s99, 0
	s_waitcnt lgkmcnt(0)
	global_store_dwordx4 v242, v[0:3], s[100:101]
	s_nop 1
	s_cbranch_vccnz .LBB0_1817
	s_andn2_b64 vcc, exec, s[4:5]
	s_cbranch_vccnz .LBB0_1816
	s_barrier
	s_branch .LBB0_1816
